# layer-1 out-proj residual epilogue: next group's residual loads requested one group ahead (two groups in flight)
# baseline (speedup 1.0000x reference)
.LBB0_2217:
	ds_read_b128 v[142:145], v138
	ds_read_b128 v[146:149], v138 offset:1024
	ds_read_b128 v[150:153], v138 offset:2048
	ds_read_b128 v[154:157], v138 offset:3072
	s_add_u32 s30, s28, 0xfff80080
	s_addc_u32 s31, s29, -1
	s_cmp_eq_u32 s56, 28
	s_cselect_b32 s31, s19, s31
	s_cselect_b32 s30, s54, s30
	s_cselect_b32 s59, s17, s55
	s_cselect_b32 s58, s34, s35
	v_lshl_add_u64 v[136:137], s[28:29], 0, v[132:133]
	s_add_i32 m0, s27, 0xc000
	ds_read_b128 v[158:161], v139
	ds_read_b128 v[162:165], v139 offset:1024
	ds_read_b128 v[166:169], v139 offset:2048
	ds_read_b128 v[170:173], v139 offset:3072
	ds_read_b128 v[174:177], v139 offset:4096
	ds_read_b128 v[178:181], v139 offset:5120
	ds_read_b128 v[182:185], v139 offset:6144
	ds_read_b128 v[186:189], v139 offset:7168
	global_load_lds_dwordx4 v[136:137], off
	v_lshl_add_u64 v[136:137], v[136:137], 0, s[2:3]
	s_add_i32 m0, s27, 0xe000
	s_nop 0
	global_load_lds_dwordx4 v[136:137], off
	s_waitcnt lgkmcnt(8)
	s_barrier
	s_waitcnt lgkmcnt(0)
	s_setprio 1
	s_waitcnt lgkmcnt(0)
	v_mfma_scale_f32_16x16x128_f8f6f4 v[126:129], v[142:149], v[158:165], v[126:129], v140, v140 op_sel_hi:[0,0,0]
	v_mfma_scale_f32_16x16x128_f8f6f4 v[122:125], v[150:157], v[158:165], v[122:125], v140, v140 op_sel_hi:[0,0,0]
	v_mfma_scale_f32_16x16x128_f8f6f4 v[190:193], v[142:149], v[166:173], v[110:113], v140, v140 op_sel_hi:[0,0,0]
	v_mfma_scale_f32_16x16x128_f8f6f4 v[194:197], v[150:157], v[166:173], v[106:109], v140, v140 op_sel_hi:[0,0,0]
	v_mfma_scale_f32_16x16x128_f8f6f4 v[198:201], v[142:149], v[174:181], v[94:97], v140, v140 op_sel_hi:[0,0,0]
	v_mfma_scale_f32_16x16x128_f8f6f4 v[202:205], v[150:157], v[174:181], v[90:93], v140, v140 op_sel_hi:[0,0,0]
	v_mfma_scale_f32_16x16x128_f8f6f4 v[206:209], v[142:149], v[182:189], v[78:81], v140, v140 op_sel_hi:[0,0,0]
	v_mfma_scale_f32_16x16x128_f8f6f4 v[210:213], v[150:157], v[182:189], v[74:77], v140, v140 op_sel_hi:[0,0,0]
	s_setprio 0
	s_barrier
	s_add_i32 s57, s49, s40
	v_lshl_add_u64 v[136:137], s[58:59], 0, v[130:131]
	s_mov_b32 m0, s57
	s_nop 1
	ds_read_b128 v[74:77], v141
	ds_read_b128 v[78:81], v141 offset:1024
	ds_read_b128 v[90:93], v141 offset:2048
	ds_read_b128 v[94:97], v141 offset:3072
	global_load_lds_dwordx4 v[136:137], off
	v_lshl_add_u64 v[106:107], v[136:137], 0, s[2:3]
	s_add_i32 m0, s57, 0x2000
	s_nop 0
	global_load_lds_dwordx4 v[106:107], off
	s_barrier
	s_waitcnt lgkmcnt(0)
	s_setprio 1
	s_waitcnt lgkmcnt(0)
	v_mfma_scale_f32_16x16x128_f8f6f4 v[118:121], v[74:81], v[158:165], v[118:121], v140, v140 op_sel_hi:[0,0,0]
	v_mfma_scale_f32_16x16x128_f8f6f4 v[114:117], v[90:97], v[158:165], v[114:117], v140, v140 op_sel_hi:[0,0,0]
	v_mfma_scale_f32_16x16x128_f8f6f4 v[158:161], v[74:81], v[166:173], v[102:105], v140, v140 op_sel_hi:[0,0,0]
	v_mfma_scale_f32_16x16x128_f8f6f4 v[162:165], v[90:97], v[166:173], v[98:101], v140, v140 op_sel_hi:[0,0,0]
	v_mfma_scale_f32_16x16x128_f8f6f4 v[166:169], v[74:81], v[174:181], v[86:89], v140, v140 op_sel_hi:[0,0,0]
	v_mfma_scale_f32_16x16x128_f8f6f4 v[170:173], v[90:97], v[174:181], v[82:85], v140, v140 op_sel_hi:[0,0,0]
	v_mfma_scale_f32_16x16x128_f8f6f4 v[174:177], v[74:81], v[182:189], v[70:73], v140, v140 op_sel_hi:[0,0,0]
	v_mfma_scale_f32_16x16x128_f8f6f4 v[178:181], v[90:97], v[182:189], v[66:69], v140, v140 op_sel_hi:[0,0,0]
	s_setprio 0
	s_mov_b32 m0, s27
	v_lshl_add_u64 v[134:135], s[30:31], 0, v[130:131]
	s_barrier
	s_nop 2
	ds_read_b128 v[66:69], v139 offset:16384
	ds_read_b128 v[70:73], v139 offset:17408
	ds_read_b128 v[82:85], v139 offset:18432
	ds_read_b128 v[86:89], v139 offset:19456
	ds_read_b128 v[98:101], v139 offset:20480
	ds_read_b128 v[102:105], v139 offset:21504
	ds_read_b128 v[106:109], v139 offset:22528
	ds_read_b128 v[110:113], v139 offset:23552
	global_load_lds_dwordx4 v[134:135], off
	v_lshl_add_u64 v[182:183], v[134:135], 0, s[2:3]
	s_mov_b32 m0, s41
	s_nop 0
	global_load_lds_dwordx4 v[182:183], off
	s_barrier
	s_waitcnt lgkmcnt(0)
	s_setprio 1
	s_waitcnt lgkmcnt(0)
	v_mfma_scale_f32_16x16x128_f8f6f4 v[62:65], v[142:149], v[66:73], v[62:65], v140, v140 op_sel_hi:[0,0,0]
	v_mfma_scale_f32_16x16x128_f8f6f4 v[58:61], v[150:157], v[66:73], v[58:61], v140, v140 op_sel_hi:[0,0,0]
	v_mfma_scale_f32_16x16x128_f8f6f4 v[182:185], v[142:149], v[82:89], v[46:49], v140, v140 op_sel_hi:[0,0,0]
	v_mfma_scale_f32_16x16x128_f8f6f4 v[186:189], v[150:157], v[82:89], v[42:45], v140, v140 op_sel_hi:[0,0,0]
	v_mfma_scale_f32_16x16x128_f8f6f4 v[214:217], v[142:149], v[98:105], v[30:33], v140, v140 op_sel_hi:[0,0,0]
	v_mfma_scale_f32_16x16x128_f8f6f4 v[218:221], v[150:157], v[98:105], v[26:29], v140, v140 op_sel_hi:[0,0,0]
	v_mfma_scale_f32_16x16x128_f8f6f4 v[222:225], v[142:149], v[106:113], v[14:17], v140, v140 op_sel_hi:[0,0,0]
	v_mfma_scale_f32_16x16x128_f8f6f4 v[226:229], v[150:157], v[106:113], v[10:13], v140, v140 op_sel_hi:[0,0,0]
	s_setprio 0
	s_barrier
	s_add_i32 s30, s50, s40
	s_nop 3
	v_lshl_add_u64 v[10:11], v[136:137], 0, s[4:5]
	s_mov_b32 m0, s30
	s_nop 0
	global_load_lds_dwordx4 v[10:11], off
	v_lshl_add_u64 v[10:11], v[136:137], 0, s[6:7]
	s_add_i32 m0, s30, 0x2000
	s_nop 0
	global_load_lds_dwordx4 v[10:11], off
	s_waitcnt vmcnt(6)
	s_barrier
	s_setprio 1
	v_mfma_scale_f32_16x16x128_f8f6f4 v[54:57], v[74:81], v[66:73], v[54:57], v140, v140 op_sel_hi:[0,0,0]
	v_mfma_scale_f32_16x16x128_f8f6f4 v[50:53], v[90:97], v[66:73], v[50:53], v140, v140 op_sel_hi:[0,0,0]
	v_mfma_scale_f32_16x16x128_f8f6f4 v[230:233], v[74:81], v[82:89], v[38:41], v140, v140 op_sel_hi:[0,0,0]
	v_mfma_scale_f32_16x16x128_f8f6f4 v[234:237], v[90:97], v[82:89], v[34:37], v140, v140 op_sel_hi:[0,0,0]
	v_mfma_scale_f32_16x16x128_f8f6f4 v[238:241], v[74:81], v[98:105], v[22:25], v140, v140 op_sel_hi:[0,0,0]
	v_mfma_scale_f32_16x16x128_f8f6f4 v[242:245], v[90:97], v[98:105], v[18:21], v140, v140 op_sel_hi:[0,0,0]
	v_mfma_scale_f32_16x16x128_f8f6f4 v[246:249], v[74:81], v[106:113], v[6:9], v140, v140 op_sel_hi:[0,0,0]
	v_mfma_scale_f32_16x16x128_f8f6f4 v[250:253], v[90:97], v[106:113], v[2:5], v140, v140 op_sel_hi:[0,0,0]
	s_setprio 0
	s_add_i32 s30, 0, 0x18000
	v_add_u32_e32 v10, s30, v1
	s_barrier
	s_nop 2
	ds_read_b128 v[2:5], v10
	ds_read_b128 v[6:9], v10 offset:1024
	ds_read_b128 v[18:21], v10 offset:2048
	ds_read_b128 v[22:25], v10 offset:3072
	s_mov_b32 m0, s42
	v_lshl_add_u64 v[66:67], v[134:135], 0, s[4:5]
	ds_read_b128 v[10:13], v139 offset:32768
	ds_read_b128 v[14:17], v139 offset:33792
	ds_read_b128 v[26:29], v139 offset:34816
	ds_read_b128 v[30:33], v139 offset:35840
	ds_read_b128 v[34:37], v139 offset:36864
	ds_read_b128 v[38:41], v139 offset:37888
	ds_read_b128 v[42:45], v139 offset:38912
	ds_read_b128 v[46:49], v139 offset:39936
	global_load_lds_dwordx4 v[66:67], off
	v_lshl_add_u64 v[66:67], v[134:135], 0, s[6:7]
	s_mov_b32 m0, s43
	s_nop 0
	global_load_lds_dwordx4 v[66:67], off
	s_waitcnt lgkmcnt(8)
	s_barrier
	s_waitcnt lgkmcnt(0)
	s_setprio 1
	s_waitcnt lgkmcnt(0)
	v_mfma_scale_f32_16x16x128_f8f6f4 v[126:129], v[2:9], v[10:17], v[126:129], v140, v140 op_sel_hi:[0,0,0]
	v_mfma_scale_f32_16x16x128_f8f6f4 v[122:125], v[18:25], v[10:17], v[122:125], v140, v140 op_sel_hi:[0,0,0]
	v_mfma_scale_f32_16x16x128_f8f6f4 v[110:113], v[2:9], v[26:33], v[190:193], v140, v140 op_sel_hi:[0,0,0]
	v_mfma_scale_f32_16x16x128_f8f6f4 v[106:109], v[18:25], v[26:33], v[194:197], v140, v140 op_sel_hi:[0,0,0]
	v_mfma_scale_f32_16x16x128_f8f6f4 v[94:97], v[2:9], v[34:41], v[198:201], v140, v140 op_sel_hi:[0,0,0]
	v_mfma_scale_f32_16x16x128_f8f6f4 v[90:93], v[18:25], v[34:41], v[202:205], v140, v140 op_sel_hi:[0,0,0]
	v_mfma_scale_f32_16x16x128_f8f6f4 v[78:81], v[2:9], v[42:49], v[206:209], v140, v140 op_sel_hi:[0,0,0]
	v_mfma_scale_f32_16x16x128_f8f6f4 v[74:77], v[18:25], v[42:49], v[210:213], v140, v140 op_sel_hi:[0,0,0]
	s_setprio 0
	s_barrier
	s_add_i32 s31, 0, 0x1c000
	v_add_u32_e32 v66, s31, v1
	s_add_i32 s30, s30, s40
	ds_read_b128 v[142:145], v66
	ds_read_b128 v[146:149], v66 offset:1024
	ds_read_b128 v[150:153], v66 offset:2048
	ds_read_b128 v[154:157], v66 offset:3072
	v_lshl_add_u64 v[66:67], v[136:137], 0, s[8:9]
	s_mov_b32 m0, s30
	s_nop 0
	global_load_lds_dwordx4 v[66:67], off
	v_lshl_add_u64 v[66:67], v[136:137], 0, s[10:11]
	s_add_i32 m0, s30, 0x2000
	s_nop 0
	global_load_lds_dwordx4 v[66:67], off
	s_barrier
	s_waitcnt lgkmcnt(0)
	s_setprio 1
	s_waitcnt lgkmcnt(0)
	v_mfma_scale_f32_16x16x128_f8f6f4 v[118:121], v[142:149], v[10:17], v[118:121], v140, v140 op_sel_hi:[0,0,0]
	v_mfma_scale_f32_16x16x128_f8f6f4 v[114:117], v[150:157], v[10:17], v[114:117], v140, v140 op_sel_hi:[0,0,0]
	v_mfma_scale_f32_16x16x128_f8f6f4 v[102:105], v[142:149], v[26:33], v[158:161], v140, v140 op_sel_hi:[0,0,0]
	v_mfma_scale_f32_16x16x128_f8f6f4 v[98:101], v[150:157], v[26:33], v[162:165], v140, v140 op_sel_hi:[0,0,0]
	v_mfma_scale_f32_16x16x128_f8f6f4 v[86:89], v[142:149], v[34:41], v[166:169], v140, v140 op_sel_hi:[0,0,0]
	v_mfma_scale_f32_16x16x128_f8f6f4 v[82:85], v[150:157], v[34:41], v[170:173], v140, v140 op_sel_hi:[0,0,0]
	v_mfma_scale_f32_16x16x128_f8f6f4 v[70:73], v[142:149], v[42:49], v[174:177], v140, v140 op_sel_hi:[0,0,0]
	v_mfma_scale_f32_16x16x128_f8f6f4 v[66:69], v[150:157], v[42:49], v[178:181], v140, v140 op_sel_hi:[0,0,0]
	s_setprio 0
	s_mov_b32 m0, s45
	v_lshl_add_u64 v[10:11], v[134:135], 0, s[8:9]
	s_barrier
	ds_read_b128 v[34:37], v139 offset:49152
	ds_read_b128 v[38:41], v139 offset:50176
	ds_read_b128 v[158:161], v139 offset:51200
	ds_read_b128 v[162:165], v139 offset:52224
	ds_read_b128 v[166:169], v139 offset:53248
	ds_read_b128 v[170:173], v139 offset:54272
	ds_read_b128 v[174:177], v139 offset:55296
	ds_read_b128 v[178:181], v139 offset:56320
	global_load_lds_dwordx4 v[10:11], off
	v_lshl_add_u64 v[10:11], v[134:135], 0, s[10:11]
	s_mov_b32 m0, s46
	s_nop 0
	global_load_lds_dwordx4 v[10:11], off
	s_barrier
	s_waitcnt lgkmcnt(0)
	s_setprio 1
	s_waitcnt lgkmcnt(0)
	v_mfma_scale_f32_16x16x128_f8f6f4 v[62:65], v[2:9], v[34:41], v[62:65], v140, v140 op_sel_hi:[0,0,0]
	v_mfma_scale_f32_16x16x128_f8f6f4 v[58:61], v[18:25], v[34:41], v[58:61], v140, v140 op_sel_hi:[0,0,0]
	v_mfma_scale_f32_16x16x128_f8f6f4 v[46:49], v[2:9], v[158:165], v[182:185], v140, v140 op_sel_hi:[0,0,0]
	v_mfma_scale_f32_16x16x128_f8f6f4 v[42:45], v[18:25], v[158:165], v[186:189], v140, v140 op_sel_hi:[0,0,0]
	v_mfma_scale_f32_16x16x128_f8f6f4 v[30:33], v[2:9], v[166:173], v[214:217], v140, v140 op_sel_hi:[0,0,0]
	v_mfma_scale_f32_16x16x128_f8f6f4 v[26:29], v[18:25], v[166:173], v[218:221], v140, v140 op_sel_hi:[0,0,0]
	v_mfma_scale_f32_16x16x128_f8f6f4 v[14:17], v[2:9], v[174:181], v[222:225], v140, v140 op_sel_hi:[0,0,0]
	v_mfma_scale_f32_16x16x128_f8f6f4 v[10:13], v[18:25], v[174:181], v[226:229], v140, v140 op_sel_hi:[0,0,0]
	s_setprio 0
	s_barrier
	s_add_i32 s30, s31, s40
	v_lshl_add_u64 v[2:3], v[136:137], 0, s[12:13]
	s_mov_b32 m0, s30
	s_nop 0
	global_load_lds_dwordx4 v[2:3], off
	v_lshl_add_u64 v[2:3], v[136:137], 0, s[14:15]
	s_add_i32 m0, s30, 0x2000
	s_nop 0
	global_load_lds_dwordx4 v[2:3], off
	s_waitcnt vmcnt(6)
	s_barrier
	s_setprio 1
	v_mfma_scale_f32_16x16x128_f8f6f4 v[54:57], v[142:149], v[34:41], v[54:57], v140, v140 op_sel_hi:[0,0,0]
	v_mfma_scale_f32_16x16x128_f8f6f4 v[50:53], v[150:157], v[34:41], v[50:53], v140, v140 op_sel_hi:[0,0,0]
	v_mfma_scale_f32_16x16x128_f8f6f4 v[38:41], v[142:149], v[158:165], v[230:233], v140, v140 op_sel_hi:[0,0,0]
	v_mfma_scale_f32_16x16x128_f8f6f4 v[34:37], v[150:157], v[158:165], v[234:237], v140, v140 op_sel_hi:[0,0,0]
	v_mfma_scale_f32_16x16x128_f8f6f4 v[22:25], v[142:149], v[166:173], v[238:241], v140, v140 op_sel_hi:[0,0,0]
	v_mfma_scale_f32_16x16x128_f8f6f4 v[18:21], v[150:157], v[166:173], v[242:245], v140, v140 op_sel_hi:[0,0,0]
	v_mfma_scale_f32_16x16x128_f8f6f4 v[6:9], v[142:149], v[174:181], v[246:249], v140, v140 op_sel_hi:[0,0,0]
	v_mfma_scale_f32_16x16x128_f8f6f4 v[2:5], v[150:157], v[174:181], v[250:253], v140, v140 op_sel_hi:[0,0,0]
	s_setprio 0
	s_add_i32 s56, s56, 2
	s_add_u32 s28, s28, 0x100
	s_addc_u32 s29, s29, 0
	s_add_u32 s35, s35, 0x100
	s_addc_u32 s55, s55, 0
	s_cmp_gt_u32 s56, 29
	s_barrier
	s_cbranch_scc0 .LBB0_2217
	v_mov_b32_e32 v134, v0
	s_lshl_b32 s17, s26, 8
	v_readlane_b32 s56, v254, 18
	v_ashrrev_i32_e32 v135, 8, v134
	v_bfe_u32 v137, v134, 6, 2
	v_lshlrev_b32_e32 v144, 4, v134
	v_bfe_u32 v142, v134, 2, 4
	v_lshl_add_u32 v136, v135, 6, s17
	s_lshl_b32 s17, s53, 10
	v_lshlrev_b32_e32 v143, 7, v137
	v_and_b32_e32 v160, 48, v144
	v_or_b32_e32 v136, v136, v142
	v_or3_b32 v143, v143, s17, v160
	v_lshl_add_u32 v136, v136, 13, v143
	v_readlane_b32 s70, v254, 32
	v_readlane_b32 s71, v254, 33
	s_nop 4
	global_load_dwordx4 v[144:147], v136, s[70:71]
	global_load_dwordx4 v[148:151], v136, s[70:71] offset:64
	global_load_dwordx4 v[152:155], v136, s[70:71] offset:512
	global_load_dwordx4 v[156:159], v136, s[70:71] offset:576
	v_lshl_or_b32 v135, v135, 2, v137
	v_and_b32_e32 v143, 15, v134
	v_mul_lo_u32 v135, v135, s51
	v_and_b32_e32 v134, 48, v134
	v_mul_u32_u24_e32 v137, 0x50, v143
	v_add_u32_e32 v135, s52, v135
	v_mul_u32_u24_e32 v142, 0x50, v142
	v_add3_u32 v137, v135, v137, v134
	v_add3_u32 v142, v135, v142, v160
	ds_write_b128 v137, v[126:129]
	ds_read_b128 v[126:129], v142
	ds_write_b128 v137, v[122:125] offset:1280
	ds_read_b128 v[122:125], v142 offset:1280
	ds_write_b128 v137, v[118:121]
	ds_read_b128 v[118:121], v142
	ds_write_b128 v137, v[114:117] offset:1280
	ds_read_b128 v[114:117], v142 offset:1280
	v_readlane_b32 s57, v254, 19
	v_readlane_b32 s58, v254, 20
	v_readlane_b32 s59, v254, 21
	v_readlane_b32 s60, v254, 22
	v_readlane_b32 s61, v254, 23
	v_readlane_b32 s62, v254, 24
	v_readlane_b32 s63, v254, 25
	v_readlane_b32 s64, v254, 26
	v_readlane_b32 s65, v254, 27
	v_readlane_b32 s66, v254, 28
	v_readlane_b32 s67, v254, 29
	v_readlane_b32 s68, v254, 30
	v_readlane_b32 s69, v254, 31
	v_add_u32_e32 v196, 0x20000, v136
	global_load_dwordx4 v[164:167], v196, s[70:71]
	v_add_u32_e32 v197, 0x20040, v136
	v_add_u32_e32 v198, 0x20200, v136
	v_add_u32_e32 v199, 0x20240, v136
	global_load_dwordx4 v[168:171], v197, s[70:71]
	global_load_dwordx4 v[172:175], v198, s[70:71]
	global_load_dwordx4 v[176:179], v199, s[70:71]
	s_waitcnt vmcnt(4) lgkmcnt(0)
	v_pk_add_f32 v[128:129], v[128:129], v[146:147]
	v_pk_add_f32 v[126:127], v[126:127], v[144:145]
	v_pk_add_f32 v[124:125], v[124:125], v[150:151]
	v_pk_add_f32 v[122:123], v[122:123], v[148:149]
	v_pk_add_f32 v[120:121], v[120:121], v[154:155]
	v_pk_add_f32 v[118:119], v[118:119], v[152:153]
	v_pk_add_f32 v[116:117], v[116:117], v[158:159]
	v_pk_add_f32 v[114:115], v[114:115], v[156:157]
	global_store_dwordx4 v136, v[126:129], s[70:71]
	global_store_dwordx4 v136, v[122:125], s[70:71] offset:64
	global_store_dwordx4 v136, v[118:121], s[70:71] offset:512
	global_store_dwordx4 v136, v[114:117], s[70:71] offset:576
	s_nop 1
	v_add_u32_e32 v114, 0x40000, v136
	global_load_dwordx4 v[180:183], v114, s[70:71]
	v_add_u32_e32 v115, 0x40040, v136
	v_add_u32_e32 v116, 0x40200, v136
	v_add_u32_e32 v117, 0x40240, v136
	global_load_dwordx4 v[184:187], v115, s[70:71]
	global_load_dwordx4 v[188:191], v116, s[70:71]
	global_load_dwordx4 v[192:195], v117, s[70:71]
	ds_write_b128 v137, v[110:113]
	ds_read_b128 v[110:113], v142
	ds_write_b128 v137, v[106:109] offset:1280
	ds_read_b128 v[106:109], v142 offset:1280
	ds_write_b128 v137, v[102:105]
	ds_read_b128 v[102:105], v142
	ds_write_b128 v137, v[98:101] offset:1280
	ds_read_b128 v[98:101], v142 offset:1280
	s_waitcnt vmcnt(11) lgkmcnt(6)
	v_pk_add_f32 v[112:113], v[112:113], v[166:167]
	v_pk_add_f32 v[110:111], v[110:111], v[164:165]
	s_waitcnt vmcnt(10) lgkmcnt(4)
	v_pk_add_f32 v[108:109], v[108:109], v[170:171]
	v_pk_add_f32 v[106:107], v[106:107], v[168:169]
	s_waitcnt vmcnt(9) lgkmcnt(2)
	v_pk_add_f32 v[104:105], v[104:105], v[174:175]
	v_pk_add_f32 v[102:103], v[102:103], v[172:173]
	s_waitcnt vmcnt(8) lgkmcnt(0)
	v_pk_add_f32 v[100:101], v[100:101], v[178:179]
	v_pk_add_f32 v[98:99], v[98:99], v[176:177]
	global_store_dwordx4 v196, v[110:113], s[70:71]
	global_store_dwordx4 v197, v[106:109], s[70:71]
	global_store_dwordx4 v198, v[102:105], s[70:71]
	global_store_dwordx4 v199, v[98:101], s[70:71]
	s_nop 1
	v_add_u32_e32 v98, 0x60000, v136
	global_load_dwordx4 v[164:167], v98, s[70:71]
	v_add_u32_e32 v99, 0x60040, v136
	v_add_u32_e32 v100, 0x60200, v136
	v_add_u32_e32 v101, 0x60240, v136
	global_load_dwordx4 v[168:171], v99, s[70:71]
	global_load_dwordx4 v[172:175], v100, s[70:71]
	global_load_dwordx4 v[176:179], v101, s[70:71]
	ds_write_b128 v137, v[94:97]
	ds_read_b128 v[94:97], v142
	ds_write_b128 v137, v[90:93] offset:1280
	ds_read_b128 v[90:93], v142 offset:1280
	ds_write_b128 v137, v[86:89]
	ds_read_b128 v[86:89], v142
	ds_write_b128 v137, v[82:85] offset:1280
	ds_read_b128 v[82:85], v142 offset:1280
	s_waitcnt vmcnt(11) lgkmcnt(6)
	v_pk_add_f32 v[96:97], v[96:97], v[182:183]
	v_pk_add_f32 v[94:95], v[94:95], v[180:181]
	s_waitcnt vmcnt(10) lgkmcnt(4)
	v_pk_add_f32 v[92:93], v[92:93], v[186:187]
	v_pk_add_f32 v[90:91], v[90:91], v[184:185]
	s_waitcnt vmcnt(9) lgkmcnt(2)
	v_pk_add_f32 v[88:89], v[88:89], v[190:191]
	v_pk_add_f32 v[86:87], v[86:87], v[188:189]
	s_waitcnt vmcnt(8) lgkmcnt(0)
	v_pk_add_f32 v[84:85], v[84:85], v[194:195]
	v_pk_add_f32 v[82:83], v[82:83], v[192:193]
	global_store_dwordx4 v114, v[94:97], s[70:71]
	global_store_dwordx4 v115, v[90:93], s[70:71]
	global_store_dwordx4 v116, v[86:89], s[70:71]
	global_store_dwordx4 v117, v[82:85], s[70:71]
	s_nop 1
	v_add_u32_e32 v82, 0x100000, v136
	global_load_dwordx4 v[180:183], v82, s[70:71]
	v_add_u32_e32 v83, 0x100040, v136
	v_add_u32_e32 v84, 0x100200, v136
	v_add_u32_e32 v85, 0x100240, v136
	global_load_dwordx4 v[184:187], v83, s[70:71]
	global_load_dwordx4 v[188:191], v84, s[70:71]
	global_load_dwordx4 v[192:195], v85, s[70:71]
	ds_write_b128 v137, v[78:81]
	ds_read_b128 v[78:81], v142
	ds_write_b128 v137, v[74:77] offset:1280
	ds_read_b128 v[74:77], v142 offset:1280
	ds_write_b128 v137, v[70:73]
	ds_read_b128 v[70:73], v142
	ds_write_b128 v137, v[66:69] offset:1280
	ds_read_b128 v[66:69], v142 offset:1280
	s_waitcnt vmcnt(11) lgkmcnt(6)
	v_pk_add_f32 v[80:81], v[80:81], v[166:167]
	v_pk_add_f32 v[78:79], v[78:79], v[164:165]
	s_waitcnt vmcnt(10) lgkmcnt(4)
	v_pk_add_f32 v[76:77], v[76:77], v[170:171]
	v_pk_add_f32 v[74:75], v[74:75], v[168:169]
	s_waitcnt vmcnt(9) lgkmcnt(2)
	v_pk_add_f32 v[72:73], v[72:73], v[174:175]
	v_pk_add_f32 v[70:71], v[70:71], v[172:173]
	s_waitcnt vmcnt(8) lgkmcnt(0)
	v_pk_add_f32 v[68:69], v[68:69], v[178:179]
	v_pk_add_f32 v[66:67], v[66:67], v[176:177]
	global_store_dwordx4 v98, v[78:81], s[70:71]
	global_store_dwordx4 v99, v[74:77], s[70:71]
	global_store_dwordx4 v100, v[70:73], s[70:71]
	global_store_dwordx4 v101, v[66:69], s[70:71]
	s_nop 1
	v_add_u32_e32 v66, 0x120000, v136
	global_load_dwordx4 v[164:167], v66, s[70:71]
	v_add_u32_e32 v67, 0x120040, v136
	v_add_u32_e32 v68, 0x120200, v136
	v_add_u32_e32 v69, 0x120240, v136
	global_load_dwordx4 v[168:171], v67, s[70:71]
	global_load_dwordx4 v[172:175], v68, s[70:71]
	global_load_dwordx4 v[176:179], v69, s[70:71]
	ds_write_b128 v137, v[62:65]
	ds_read_b128 v[62:65], v142
	ds_write_b128 v137, v[58:61] offset:1280
	ds_read_b128 v[58:61], v142 offset:1280
	ds_write_b128 v137, v[54:57]
	ds_read_b128 v[54:57], v142
	ds_write_b128 v137, v[50:53] offset:1280
	ds_read_b128 v[50:53], v142 offset:1280
	s_waitcnt vmcnt(11) lgkmcnt(6)
	v_pk_add_f32 v[64:65], v[64:65], v[182:183]
	v_pk_add_f32 v[62:63], v[62:63], v[180:181]
	s_waitcnt vmcnt(10) lgkmcnt(4)
	v_pk_add_f32 v[60:61], v[60:61], v[186:187]
	v_pk_add_f32 v[58:59], v[58:59], v[184:185]
	s_waitcnt vmcnt(9) lgkmcnt(2)
	v_pk_add_f32 v[56:57], v[56:57], v[190:191]
	v_pk_add_f32 v[54:55], v[54:55], v[188:189]
	s_waitcnt vmcnt(8) lgkmcnt(0)
	v_pk_add_f32 v[52:53], v[52:53], v[194:195]
	v_pk_add_f32 v[50:51], v[50:51], v[192:193]
	global_store_dwordx4 v82, v[62:65], s[70:71]
	global_store_dwordx4 v83, v[58:61], s[70:71]
	global_store_dwordx4 v84, v[54:57], s[70:71]
	global_store_dwordx4 v85, v[50:53], s[70:71]
	s_nop 1
	v_add_u32_e32 v50, 0x140000, v136
	global_load_dwordx4 v[180:183], v50, s[70:71]
	v_add_u32_e32 v51, 0x140040, v136
	v_add_u32_e32 v52, 0x140200, v136
	v_add_u32_e32 v53, 0x140240, v136
	global_load_dwordx4 v[184:187], v51, s[70:71]
	global_load_dwordx4 v[188:191], v52, s[70:71]
	global_load_dwordx4 v[192:195], v53, s[70:71]
	ds_write_b128 v137, v[46:49]
	ds_read_b128 v[46:49], v142
	ds_write_b128 v137, v[42:45] offset:1280
	ds_read_b128 v[42:45], v142 offset:1280
	ds_write_b128 v137, v[38:41]
	ds_read_b128 v[38:41], v142
	ds_write_b128 v137, v[34:37] offset:1280
	ds_read_b128 v[34:37], v142 offset:1280
	s_waitcnt vmcnt(11) lgkmcnt(6)
	v_pk_add_f32 v[48:49], v[48:49], v[166:167]
	v_pk_add_f32 v[46:47], v[46:47], v[164:165]
	s_waitcnt vmcnt(10) lgkmcnt(4)
	v_pk_add_f32 v[44:45], v[44:45], v[170:171]
	v_pk_add_f32 v[42:43], v[42:43], v[168:169]
	s_waitcnt vmcnt(9) lgkmcnt(2)
	v_pk_add_f32 v[40:41], v[40:41], v[174:175]
	v_pk_add_f32 v[38:39], v[38:39], v[172:173]
	s_waitcnt vmcnt(8) lgkmcnt(0)
	v_pk_add_f32 v[36:37], v[36:37], v[178:179]
	v_pk_add_f32 v[34:35], v[34:35], v[176:177]
	global_store_dwordx4 v66, v[46:49], s[70:71]
	global_store_dwordx4 v67, v[42:45], s[70:71]
	global_store_dwordx4 v68, v[38:41], s[70:71]
	global_store_dwordx4 v69, v[34:37], s[70:71]
	s_nop 1
	v_add_u32_e32 v34, 0x160000, v136
	global_load_dwordx4 v[164:167], v34, s[70:71]
	v_add_u32_e32 v35, 0x160040, v136
	v_add_u32_e32 v36, 0x160200, v136
	v_add_u32_e32 v37, 0x160240, v136
	global_load_dwordx4 v[168:171], v35, s[70:71]
	global_load_dwordx4 v[172:175], v36, s[70:71]
	global_load_dwordx4 v[176:179], v37, s[70:71]
	ds_write_b128 v137, v[30:33]
	ds_read_b128 v[30:33], v142
	ds_write_b128 v137, v[26:29] offset:1280
	ds_read_b128 v[26:29], v142 offset:1280
	ds_write_b128 v137, v[22:25]
	ds_read_b128 v[22:25], v142
	ds_write_b128 v137, v[18:21] offset:1280
	ds_read_b128 v[18:21], v142 offset:1280
	s_waitcnt vmcnt(11) lgkmcnt(6)
	v_pk_add_f32 v[32:33], v[32:33], v[182:183]
	v_pk_add_f32 v[30:31], v[30:31], v[180:181]
	s_waitcnt vmcnt(10) lgkmcnt(4)
	v_pk_add_f32 v[28:29], v[28:29], v[186:187]
	v_pk_add_f32 v[26:27], v[26:27], v[184:185]
	s_waitcnt vmcnt(9) lgkmcnt(2)
	v_pk_add_f32 v[24:25], v[24:25], v[190:191]
	v_pk_add_f32 v[22:23], v[22:23], v[188:189]
	s_waitcnt vmcnt(8) lgkmcnt(0)
	v_pk_add_f32 v[20:21], v[20:21], v[194:195]
	v_pk_add_f32 v[18:19], v[18:19], v[192:193]
	global_store_dwordx4 v50, v[30:33], s[70:71]
	global_store_dwordx4 v51, v[26:29], s[70:71]
	global_store_dwordx4 v52, v[22:25], s[70:71]
	global_store_dwordx4 v53, v[18:21], s[70:71]
	ds_write_b128 v137, v[14:17]
	ds_read_b128 v[14:17], v142
	ds_write_b128 v137, v[10:13] offset:1280
	ds_read_b128 v[10:13], v142 offset:1280
	ds_write_b128 v137, v[6:9]
	ds_read_b128 v[6:9], v142
	ds_write_b128 v137, v[2:5] offset:1280
	ds_read_b128 v[2:5], v142 offset:1280
	s_waitcnt vmcnt(7) lgkmcnt(6)
	v_pk_add_f32 v[16:17], v[16:17], v[166:167]
	v_pk_add_f32 v[14:15], v[14:15], v[164:165]
	s_waitcnt vmcnt(6) lgkmcnt(4)
	v_pk_add_f32 v[12:13], v[12:13], v[170:171]
	v_pk_add_f32 v[10:11], v[10:11], v[168:169]
	s_waitcnt vmcnt(5) lgkmcnt(2)
	v_pk_add_f32 v[8:9], v[8:9], v[174:175]
	v_pk_add_f32 v[6:7], v[6:7], v[172:173]
	s_waitcnt vmcnt(4) lgkmcnt(0)
	v_pk_add_f32 v[4:5], v[4:5], v[178:179]
	v_pk_add_f32 v[2:3], v[2:3], v[176:177]
	global_store_dwordx4 v34, v[14:17], s[70:71]
	global_store_dwordx4 v35, v[10:13], s[70:71]
	global_store_dwordx4 v36, v[6:9], s[70:71]
	global_store_dwordx4 v37, v[2:5], s[70:71]
	s_and_b64 vcc, exec, s[22:23]
	s_mov_b32 s53, s16
	s_mov_b32 s26, s18
	s_mov_b64 s[30:31], s[24:25]
	s_mov_b64 s[28:29], s[20:21]
	s_cbranch_vccz .LBB0_2209
	s_waitcnt vmcnt(0)
	s_cmpk_gt_u32 s33, 0xff
	s_cbranch_scc1 .LBB0_2221
	s_barrier
